# attention fast loop: s_setprio 1 around the 12-MFMA PV cluster (on top of SrcC init change)
# baseline (speedup 1.0000x reference)
.LBB0_393:
	v_add_u32_e32 v67, s1, v203
	ds_read_b64_tr_b16 v[102:103], v67 offset:0
	ds_read_b64_tr_b16 v[104:105], v67 offset:0x800
	ds_read_b64_tr_b16 v[106:107], v67 offset:0x1000
	ds_read_b64_tr_b16 v[108:109], v67 offset:0x1800
	ds_read_b64_tr_b16 v[110:111], v67 offset:0x2000
	ds_read_b64_tr_b16 v[112:113], v67 offset:0x2800
	ds_read_b64_tr_b16 v[164:165], v67 offset:0x3000
	ds_read_b64_tr_b16 v[166:167], v67 offset:0x3800
	ds_read_b64_tr_b16 v[178:179], v67 offset:0x200
	ds_read_b64_tr_b16 v[180:181], v67 offset:0xa00
	ds_read_b64_tr_b16 v[182:183], v67 offset:0x1200
	ds_read_b64_tr_b16 v[184:185], v67 offset:0x1a00
	ds_read_b64_tr_b16 v[186:187], v67 offset:0x2200
	ds_read_b64_tr_b16 v[188:189], v67 offset:0x2a00
	ds_read_b64_tr_b16 v[190:191], v67 offset:0x3200
	ds_read_b64_tr_b16 v[192:193], v67 offset:0x3a00
	s_nop 0
	s_waitcnt lgkmcnt(8)
	ds_read_b64_tr_b16 v[206:207], v67 offset:0x400
	ds_read_b64_tr_b16 v[208:209], v67 offset:0xc00
	ds_read_b64_tr_b16 v[210:211], v67 offset:0x1400
	ds_read_b64_tr_b16 v[212:213], v67 offset:0x1c00
	ds_read_b64_tr_b16 v[214:215], v67 offset:0x2400
	s_nop 0
	s_setprio 1
	v_mfma_f32_32x32x16_bf16 v[2:17], v[68:71], v[102:105], v[2:17]
	ds_read_b64_tr_b16 v[216:217], v67 offset:0x2c00
	ds_read_b64_tr_b16 v[218:219], v67 offset:0x3400
	ds_read_b64_tr_b16 v[220:221], v67 offset:0x3c00
	s_waitcnt lgkmcnt(8)
	s_and_b64 vcc, exec, s[40:41]
	v_mfma_f32_32x32x16_bf16 v[2:17], v[78:81], v[106:109], v[2:17]
	v_mfma_f32_32x32x16_bf16 v[2:17], v[74:77], v[110:113], v[2:17]
	v_mfma_f32_32x32x16_bf16 v[2:17], v[98:101], v[164:167], v[2:17]
	ds_read_b64_tr_b16 v[164:165], v67 offset:0x600
	ds_read_b64_tr_b16 v[166:167], v67 offset:0xe00
	ds_read_b64_tr_b16 v[110:111], v67 offset:0x1600
	ds_read_b64_tr_b16 v[112:113], v67 offset:0x1e00
	ds_read_b64_tr_b16 v[106:107], v67 offset:0x2600
	ds_read_b64_tr_b16 v[108:109], v67 offset:0x2e00
	ds_read_b64_tr_b16 v[102:103], v67 offset:0x3600
	ds_read_b64_tr_b16 v[104:105], v67 offset:0x3e00
	v_mfma_f32_32x32x16_bf16 v[18:33], v[68:71], v[178:181], v[18:33]
	s_waitcnt lgkmcnt(8)
	s_waitcnt lgkmcnt(0)
	s_nop 0
	v_mfma_f32_32x32x16_bf16 v[34:49], v[68:71], v[206:209], v[34:49]
	v_mfma_f32_32x32x16_bf16 v[18:33], v[78:81], v[182:185], v[18:33]
	v_mfma_f32_32x32x16_bf16 v[34:49], v[78:81], v[210:213], v[34:49]
	v_mfma_f32_32x32x16_bf16 v[18:33], v[74:77], v[186:189], v[18:33]
	v_mfma_f32_32x32x16_bf16 v[34:49], v[74:77], v[214:217], v[34:49]
	v_mfma_f32_32x32x16_bf16 v[18:33], v[98:101], v[190:193], v[18:33]
	v_mfma_f32_32x32x16_bf16 v[34:49], v[98:101], v[218:221], v[34:49]
	s_setprio 0
	s_cbranch_vccnz .LBB0_400
	s_cmp_ge_u32 s2, s65
	s_mov_b64 s[8:9], -1
	s_cbranch_scc0 .LBB0_396
	s_waitcnt vmcnt(0) lgkmcnt(0)
	s_mov_b64 s[8:9], 0

.LBB0_409:
	v_add_u32_e32 v80, s7, v203
	ds_read_b64_tr_b16 v[118:119], v80 offset:0
	ds_read_b64_tr_b16 v[120:121], v80 offset:0x800
	ds_read_b64_tr_b16 v[122:123], v80 offset:0x1000
	ds_read_b64_tr_b16 v[124:125], v80 offset:0x1800
	ds_read_b64_tr_b16 v[126:127], v80 offset:0x2000
	ds_read_b64_tr_b16 v[128:129], v80 offset:0x2800
	ds_read_b64_tr_b16 v[164:165], v80 offset:0x3000
	ds_read_b64_tr_b16 v[166:167], v80 offset:0x3800
	ds_read_b64_tr_b16 v[178:179], v80 offset:0x200
	ds_read_b64_tr_b16 v[180:181], v80 offset:0xa00
	ds_read_b64_tr_b16 v[182:183], v80 offset:0x1200
	ds_read_b64_tr_b16 v[184:185], v80 offset:0x1a00
	ds_read_b64_tr_b16 v[186:187], v80 offset:0x2200
	ds_read_b64_tr_b16 v[188:189], v80 offset:0x2a00
	ds_read_b64_tr_b16 v[206:207], v80 offset:0x3200
	ds_read_b64_tr_b16 v[208:209], v80 offset:0x3a00
	s_nop 0
	s_waitcnt lgkmcnt(8)
	ds_read_b64_tr_b16 v[210:211], v80 offset:0x400
	ds_read_b64_tr_b16 v[212:213], v80 offset:0xc00
	ds_read_b64_tr_b16 v[214:215], v80 offset:0x1400
	ds_read_b64_tr_b16 v[216:217], v80 offset:0x1c00
	ds_read_b64_tr_b16 v[218:219], v80 offset:0x2400
	s_nop 0
	s_setprio 1
	v_mfma_f32_32x32x16_bf16 v[2:17], v[68:71], v[118:121], v[2:17]
	ds_read_b64_tr_b16 v[220:221], v80 offset:0x2c00
	ds_read_b64_tr_b16 v[222:223], v80 offset:0x3400
	ds_read_b64_tr_b16 v[224:225], v80 offset:0x3c00
	s_waitcnt lgkmcnt(8)
	s_and_b64 vcc, exec, s[40:41]
	v_mfma_f32_32x32x16_bf16 v[2:17], v[72:75], v[122:125], v[2:17]
	v_mfma_f32_32x32x16_bf16 v[2:17], v[76:79], v[126:129], v[2:17]
	ds_read_b64_tr_b16 v[126:127], v80 offset:0x600
	ds_read_b64_tr_b16 v[128:129], v80 offset:0xe00
	ds_read_b64_tr_b16 v[122:123], v80 offset:0x1600
	ds_read_b64_tr_b16 v[124:125], v80 offset:0x1e00
	ds_read_b64_tr_b16 v[118:119], v80 offset:0x2600
	ds_read_b64_tr_b16 v[120:121], v80 offset:0x2e00
	v_mfma_f32_32x32x16_bf16 v[2:17], v[114:117], v[164:167], v[2:17]
	ds_read_b64_tr_b16 v[164:165], v80 offset:0x3600
	ds_read_b64_tr_b16 v[166:167], v80 offset:0x3e00
	s_waitcnt lgkmcnt(8)
	s_nop 0
	s_waitcnt lgkmcnt(0)
	v_mfma_f32_32x32x16_bf16 v[18:33], v[68:71], v[178:181], v[18:33]
	v_mfma_f32_32x32x16_bf16 v[34:49], v[68:71], v[210:213], v[34:49]
	v_mfma_f32_32x32x16_bf16 v[18:33], v[72:75], v[182:185], v[18:33]
	v_mfma_f32_32x32x16_bf16 v[34:49], v[72:75], v[214:217], v[34:49]
	v_mfma_f32_32x32x16_bf16 v[18:33], v[76:79], v[186:189], v[18:33]
	v_mfma_f32_32x32x16_bf16 v[34:49], v[76:79], v[218:221], v[34:49]
	v_mfma_f32_32x32x16_bf16 v[18:33], v[114:117], v[206:209], v[18:33]
	v_mfma_f32_32x32x16_bf16 v[34:49], v[114:117], v[222:225], v[34:49]
	s_setprio 0
	s_cbranch_vccnz .LBB0_418
	s_cmp_ge_u32 s2, s74
	s_mov_b64 s[8:9], -1
	s_cbranch_scc0 .LBB0_412
	s_waitcnt vmcnt(0) lgkmcnt(0)
	s_mov_b64 s[8:9], 0
